# P6 epilogue: the four LayerNorm parameter rows are staged once per 4-token pass in the wave's idle LDS table region and read with ds_read_b128 instead of 16 KiB of global loads per token
# speedup vs baseline: 1.0362x; 1.0138x over previous
.LBB0_975:
	s_add_i32 s0, s96, s35
	s_ashr_i32 s1, s0, 31
	s_lshr_b32 s1, s1, 19
	s_add_i32 s0, s0, s1
	s_ashr_i32 s2, s0, 13
	s_xor_b64 s[14:15], s[6:7], -1
	s_ashr_i32 s0, s2, 31
	s_add_u32 s1, s2, s87
	s_addc_u32 s0, s0, 0
	s_waitcnt vmcnt(0)
	v_lshlrev_b32_e32 v186, 6, v179
	v_lshl_add_u32 v185, v179, 4, s85
	v_mov_b32_e32 v187, 0
	global_load_dwordx4 v[8:11], v186, s[16:17] offset:0
	global_load_dwordx4 v[12:15], v186, s[16:17] offset:16
	global_load_dwordx4 v[16:19], v186, s[16:17] offset:32
	global_load_dwordx4 v[20:23], v186, s[16:17] offset:48
	global_load_dwordx4 v[24:27], v186, s[28:29] offset:0
	global_load_dwordx4 v[28:31], v186, s[28:29] offset:16
	global_load_dwordx4 v[32:35], v186, s[28:29] offset:32
	global_load_dwordx4 v[36:39], v186, s[28:29] offset:48
	global_load_dwordx4 v[40:43], v186, s[12:13] offset:0
	global_load_dwordx4 v[44:47], v186, s[12:13] offset:16
	global_load_dwordx4 v[48:51], v186, s[12:13] offset:32
	global_load_dwordx4 v[52:55], v186, s[12:13] offset:48
	global_load_dwordx4 v[56:59], v186, s[90:91] offset:0
	global_load_dwordx4 v[60:63], v186, s[90:91] offset:16
	global_load_dwordx4 v[64:67], v186, s[90:91] offset:32
	global_load_dwordx4 v[68:71], v186, s[90:91] offset:48
	s_waitcnt vmcnt(0)
	ds_write_b128 v185, v[8:11] offset:0
	ds_write_b128 v185, v[12:15] offset:1024
	ds_write_b128 v185, v[16:19] offset:2048
	ds_write_b128 v185, v[20:23] offset:3072
	ds_write_b128 v185, v[24:27] offset:4096
	ds_write_b128 v185, v[28:31] offset:5120
	ds_write_b128 v185, v[32:35] offset:6144
	ds_write_b128 v185, v[36:39] offset:7168
	ds_write_b128 v185, v[40:43] offset:8192
	ds_write_b128 v185, v[44:47] offset:9216
	ds_write_b128 v185, v[48:51] offset:10240
	ds_write_b128 v185, v[52:55] offset:11264
	ds_write_b128 v185, v[56:59] offset:12288
	ds_write_b128 v185, v[60:63] offset:13312
	ds_write_b128 v185, v[64:67] offset:14336
	ds_write_b128 v185, v[68:71] offset:15360
	s_waitcnt lgkmcnt(0)
	v_readlane_b32 s40, v253, 62
	v_readlane_b32 s41, v253, 63
	s_lshl_b64 s[44:45], s[96:97], 12
	v_lshlrev_b32_e32 v2, 6, v179
	s_add_u32 s40, s40, s44
	s_addc_u32 s41, s41, s45
	s_add_u32 s40, s40, 0x1000
	s_addc_u32 s41, s41, 0
	global_load_dword v4, v2, s[40:41]
	s_add_u32 s40, s40, 0x1000
	s_addc_u32 s41, s41, 0
	global_load_dword v4, v2, s[40:41]
	s_add_u32 s40, s40, 0x1000
	s_addc_u32 s41, s41, 0
	global_load_dword v4, v2, s[40:41]
	v_mov_b32_e32 v1, v179
	s_mulk_i32 s0, 0x6000
	s_mul_hi_u32 s3, s1, 0x6000
	s_add_i32 s3, s3, s0
	s_mulk_i32 s1, 0x6000
	v_lshlrev_b32_e32 v20, 4, v1
	s_add_u32 s6, s70, s1
	v_readlane_b32 s36, v253, 60
	v_ashrrev_i32_e32 v21, 31, v20
	s_addc_u32 s7, s71, s3
	s_lshl_b64 s[0:1], s[96:97], 12
	v_readlane_b32 s38, v253, 62
	v_lshlrev_b64 v[22:23], 2, v[20:21]
	v_readlane_b32 s39, v253, 63
	s_add_u32 s20, s38, s0
	v_lshl_add_u64 v[68:69], s[6:7], 0, v[22:23]
	s_mov_b64 s[6:7], 0x5000
	s_addc_u32 s21, s39, s1
	v_lshl_add_u64 v[12:13], v[68:69], 0, s[6:7]
	s_lshl_b64 s[6:7], s[96:97], 3
	v_lshl_add_u64 v[32:33], s[20:21], 0, v[22:23]
	s_add_u32 s6, s64, s6
	global_load_dwordx4 v[4:7], v[12:13], off offset:48
	global_load_dwordx4 v[8:11], v[12:13], off offset:32
	s_addc_u32 s7, s65, s7
	global_load_dwordx4 v[12:15], v[12:13], off offset:16
	s_nop 0
	global_load_dwordx2 v[72:73], v3, s[6:7]
	global_load_dwordx4 v[16:19], v[32:33], off
	global_load_dwordx4 v[24:27], v[32:33], off offset:16
	global_load_dwordx4 v[28:31], v[32:33], off offset:32
	s_nop 0
	global_load_dwordx4 v[32:35], v[32:33], off offset:48
	v_lshl_add_u64 v[60:61], s[16:17], 0, v[22:23]
	v_lshl_add_u64 v[64:65], s[28:29], 0, v[22:23]
	v_add_co_u32_e32 v68, vcc, s18, v68
	ds_read_b128 v[36:39], v185 offset:7168
	global_load_dword v184, v187, s[28:29]
	ds_read_b128 v[40:43], v185 offset:3072
	global_load_dword v184, v187, s[16:17]
	ds_read_b128 v[44:47], v185 offset:2048
	global_load_dword v184, v187, s[16:17]
	ds_read_b128 v[48:51], v185 offset:6144
	global_load_dword v184, v187, s[28:29]
	ds_read_b128 v[52:55], v185 offset:5120
	global_load_dword v184, v187, s[28:29]
	ds_read_b128 v[56:59], v185 offset:1024
	global_load_dword v184, v187, s[16:17]
	s_nop 0
	ds_read_b128 v[60:63], v185 offset:0
	global_load_dword v184, v187, s[16:17]
	s_nop 0
	ds_read_b128 v[64:67], v185 offset:4096
	global_load_dword v184, v187, s[28:29]
	v_addc_co_u32_e32 v69, vcc, 0, v69, vcc
	global_load_dwordx4 v[68:71], v[68:69], off
	v_add_u32_e32 v142, 64, v183
	v_xor_b32_e32 v1, 1, v178
	v_xor_b32_e32 v2, 2, v178
	v_cmp_lt_i32_e32 vcc, v1, v142
	v_xor_b32_e32 v74, 4, v178
	v_readlane_b32 s20, v255, 42
	v_cndmask_b32_e32 v1, v178, v1, vcc
	v_cmp_lt_i32_e32 vcc, v2, v142
	v_readlane_b32 s22, v255, 44
	s_add_u32 s0, s30, s0
	v_cndmask_b32_e32 v75, v178, v2, vcc
	v_lshlrev_b32_e32 v2, 2, v1
	v_lshlrev_b32_e32 v1, 2, v75
	v_cmp_lt_i32_e32 vcc, v74, v142
	s_addc_u32 s1, s31, s1
	v_readlane_b32 s37, v253, 61
	v_readlane_b32 s40, v254, 0
	v_readlane_b32 s41, v254, 1
	v_readlane_b32 s42, v254, 2
	v_readlane_b32 s43, v254, 3
	v_readlane_b32 s44, v254, 4
	v_readlane_b32 s45, v254, 5
	v_readlane_b32 s46, v254, 6
	v_readlane_b32 s47, v254, 7
	v_readlane_b32 s48, v254, 8
	v_readlane_b32 s49, v254, 9
	v_readlane_b32 s50, v254, 10
	v_readlane_b32 s51, v254, 11
	v_readlane_b32 s21, v255, 43
	v_readlane_b32 s23, v255, 45
	s_waitcnt lgkmcnt(0)
	s_waitcnt vmcnt(14)
	v_pk_add_f32 v[12:13], v[12:13], 1.0 op_sel_hi:[1,0]
	v_pk_add_f32 v[14:15], v[14:15], 1.0 op_sel_hi:[1,0]
	s_waitcnt lgkmcnt(0)
	s_waitcnt vmcnt(12)
	v_pk_add_f32 v[18:19], v[18:19], v[72:73] op_sel_hi:[1,0] neg_lo:[0,1] neg_hi:[0,1]
	v_pk_add_f32 v[4:5], v[4:5], 1.0 op_sel_hi:[1,0]
	v_pk_mul_f32 v[18:19], v[72:73], v[18:19] op_sel:[1,0]
	s_waitcnt lgkmcnt(0)
	s_waitcnt vmcnt(9)
	v_pk_add_f32 v[32:33], v[32:33], v[72:73] op_sel_hi:[1,0] neg_lo:[0,1] neg_hi:[0,1]
	v_pk_add_f32 v[34:35], v[34:35], v[72:73] op_sel_hi:[1,0] neg_lo:[0,1] neg_hi:[0,1]
	v_pk_mul_f32 v[32:33], v[72:73], v[32:33] op_sel:[1,0]
	v_pk_mul_f32 v[34:35], v[72:73], v[34:35] op_sel:[1,0]
	s_waitcnt lgkmcnt(0)
	s_waitcnt vmcnt(7)
	v_pk_fma_f32 v[32:33], v[32:33], v[40:41], v[36:37]
	v_pk_fma_f32 v[34:35], v[34:35], v[42:43], v[38:39]
	v_pk_mul_f32 v[32:33], v[32:33], s[34:35] op_sel_hi:[1,0]
	v_pk_add_f32 v[6:7], v[6:7], 1.0 op_sel_hi:[1,0]
	v_pk_add_f32 v[24:25], v[24:25], v[72:73] op_sel_hi:[1,0] neg_lo:[0,1] neg_hi:[0,1]
	v_pk_mul_f32 v[34:35], v[34:35], s[34:35] op_sel_hi:[1,0]
	v_pk_fma_f32 v[42:43], v[138:139], v[4:5], v[32:33]
	s_waitcnt lgkmcnt(0)
	s_waitcnt vmcnt(1)
	v_pk_fma_f32 v[4:5], v[18:19], v[62:63], v[66:67]
	v_pk_add_f32 v[16:17], v[16:17], v[72:73] op_sel_hi:[1,0] neg_lo:[0,1] neg_hi:[0,1]
	v_pk_mul_f32 v[24:25], v[72:73], v[24:25] op_sel:[1,0]
	v_pk_fma_f32 v[40:41], v[140:141], v[6:7], v[34:35]
	v_pk_mul_f32 v[4:5], v[4:5], s[34:35] op_sel_hi:[1,0]
	s_waitcnt lgkmcnt(0)
	s_waitcnt vmcnt(0)
	v_pk_add_f32 v[6:7], v[70:71], 1.0 op_sel_hi:[1,0]
	v_pk_fma_f32 v[24:25], v[24:25], v[56:57], v[52:53]
	v_pk_fma_f32 v[52:53], v[128:129], v[6:7], v[4:5]
	v_pk_mul_f32 v[4:5], v[72:73], v[16:17] op_sel:[1,0]
	v_pk_add_f32 v[26:27], v[26:27], v[72:73] op_sel_hi:[1,0] neg_lo:[0,1] neg_hi:[0,1]
	v_pk_fma_f32 v[4:5], v[60:61], v[4:5], v[64:65]
	v_pk_mul_f32 v[26:27], v[72:73], v[26:27] op_sel:[1,0]
	v_pk_mul_f32 v[4:5], v[4:5], s[34:35] op_sel_hi:[1,0]
	v_pk_add_f32 v[6:7], v[68:69], 1.0 op_sel_hi:[1,0]
	v_pk_fma_f32 v[26:27], v[26:27], v[58:59], v[54:55]
	v_pk_fma_f32 v[54:55], v[126:127], v[6:7], v[4:5]
	v_pk_add_f32 v[30:31], v[30:31], v[72:73] op_sel_hi:[1,0] neg_lo:[0,1] neg_hi:[0,1]
	v_add_f32_e32 v4, 0, v54
	v_add_f32_e32 v4, v4, v55
	v_pk_mul_f32 v[30:31], v[72:73], v[30:31] op_sel:[1,0]
	v_pk_mul_f32 v[24:25], v[24:25], s[34:35] op_sel_hi:[1,0]
	v_add_f32_e32 v4, v4, v52
	v_pk_add_f32 v[28:29], v[28:29], v[72:73] op_sel_hi:[1,0] neg_lo:[0,1] neg_hi:[0,1]
	v_pk_fma_f32 v[30:31], v[30:31], v[46:47], v[50:51]
	v_pk_fma_f32 v[50:51], v[130:131], v[12:13], v[24:25]
	v_add_f32_e32 v4, v4, v53
	v_pk_mul_f32 v[28:29], v[72:73], v[28:29] op_sel:[1,0]
	v_pk_mul_f32 v[26:27], v[26:27], s[34:35] op_sel_hi:[1,0]
	v_add_f32_e32 v4, v4, v50
	v_pk_fma_f32 v[28:29], v[28:29], v[44:45], v[48:49]
	v_pk_fma_f32 v[48:49], v[132:133], v[14:15], v[26:27]
	v_add_f32_e32 v4, v4, v51
	v_pk_add_f32 v[8:9], v[8:9], 1.0 op_sel_hi:[1,0]
	v_pk_mul_f32 v[28:29], v[28:29], s[34:35] op_sel_hi:[1,0]
	v_add_f32_e32 v4, v4, v48
	v_pk_fma_f32 v[46:47], v[134:135], v[8:9], v[28:29]
	v_add_f32_e32 v4, v4, v49
	v_pk_add_f32 v[10:11], v[10:11], 1.0 op_sel_hi:[1,0]
	v_pk_mul_f32 v[30:31], v[30:31], s[34:35] op_sel_hi:[1,0]
	v_add_f32_e32 v4, v4, v46
	v_pk_fma_f32 v[44:45], v[136:137], v[10:11], v[30:31]
	v_add_f32_e32 v4, v4, v47
	v_add_f32_e32 v4, v4, v44
	v_add_f32_e32 v4, v4, v45
	v_add_f32_e32 v4, v4, v42
	v_add_f32_e32 v4, v4, v43
	v_add_f32_e32 v4, v4, v40
	v_add_f32_e32 v4, v4, v41
	ds_bpermute_b32 v5, v2, v4
	v_cndmask_b32_e32 v6, v178, v74, vcc
	v_lshlrev_b32_e32 v74, 2, v6
	v_xor_b32_e32 v6, 8, v178
	v_cmp_lt_i32_e32 vcc, v6, v142
	s_waitcnt lgkmcnt(0)
	v_add_f32_e32 v4, v4, v5
	ds_bpermute_b32 v5, v1, v4
	v_cndmask_b32_e32 v6, v178, v6, vcc
	v_lshlrev_b32_e32 v75, 2, v6
	v_xor_b32_e32 v6, 16, v178
	v_cmp_lt_i32_e32 vcc, v6, v142
	s_waitcnt lgkmcnt(0)
	v_add_f32_e32 v4, v4, v5
	ds_bpermute_b32 v5, v74, v4
	v_cndmask_b32_e32 v6, v178, v6, vcc
	v_lshlrev_b32_e32 v126, 2, v6
	v_xor_b32_e32 v6, 32, v178
	v_cmp_lt_i32_e32 vcc, v6, v142
	s_waitcnt lgkmcnt(0)
	v_add_f32_e32 v7, v4, v5
	ds_bpermute_b32 v8, v75, v7
	v_cndmask_b32_e32 v4, v178, v6, vcc
	v_lshlrev_b32_e32 v127, 2, v4
	v_lshl_add_u64 v[4:5], s[12:13], 0, v[22:23]
	v_lshl_add_u64 v[36:37], s[90:91], 0, v[22:23]
	s_waitcnt lgkmcnt(0)
	v_add_f32_e32 v24, v7, v8
	ds_bpermute_b32 v25, v126, v24
	ds_read_b128 v[16:19], v185 offset:11264
	global_load_dword v184, v187, s[12:13]
	ds_read_b128 v[12:15], v185 offset:10240
	global_load_dword v184, v187, s[12:13]
	ds_read_b128 v[8:11], v185 offset:9216
	global_load_dword v184, v187, s[12:13]
	s_nop 0
	ds_read_b128 v[4:7], v185 offset:8192
	global_load_dword v184, v187, s[12:13]
	v_lshl_add_u64 v[22:23], s[0:1], 0, v[22:23]
	v_readlane_b32 s0, v255, 23
	v_readlane_b32 s1, v255, 24
	s_waitcnt lgkmcnt(0)
	v_add_f32_e32 v56, v24, v25
	ds_read_b128 v[24:27], v185 offset:15360
	global_load_dword v184, v187, s[90:91]
	ds_read_b128 v[28:31], v185 offset:14336
	global_load_dword v184, v187, s[90:91]
	ds_read_b128 v[32:35], v185 offset:13312
	global_load_dword v184, v187, s[90:91]
	s_nop 0
	ds_read_b128 v[36:39], v185 offset:12288
	global_load_dword v184, v187, s[90:91]
	ds_bpermute_b32 v57, v127, v56
	s_waitcnt lgkmcnt(0)
	v_add_f32_e32 v56, v56, v57
	v_mul_f32_e32 v56, 0x3a800000, v56
	v_pk_add_f32 v[54:55], v[54:55], v[56:57] op_sel_hi:[1,0] neg_lo:[0,1] neg_hi:[0,1]
	v_pk_add_f32 v[52:53], v[52:53], v[56:57] op_sel_hi:[1,0] neg_lo:[0,1] neg_hi:[0,1]
	v_pk_mul_f32 v[58:59], v[54:55], v[54:55]
	v_pk_mul_f32 v[60:61], v[52:53], v[52:53]
	v_add_f32_e32 v58, v58, v59
	v_pk_add_f32 v[50:51], v[50:51], v[56:57] op_sel_hi:[1,0] neg_lo:[0,1] neg_hi:[0,1]
	v_add_f32_e32 v58, v60, v58
	v_pk_mul_f32 v[62:63], v[50:51], v[50:51]
	v_add_f32_e32 v58, v61, v58
	v_pk_add_f32 v[48:49], v[48:49], v[56:57] op_sel_hi:[1,0] neg_lo:[0,1] neg_hi:[0,1]
	v_add_f32_e32 v58, v62, v58
	v_pk_mul_f32 v[64:65], v[48:49], v[48:49]
	v_add_f32_e32 v58, v63, v58
	v_pk_add_f32 v[46:47], v[46:47], v[56:57] op_sel_hi:[1,0] neg_lo:[0,1] neg_hi:[0,1]
	v_add_f32_e32 v58, v64, v58
	v_pk_mul_f32 v[66:67], v[46:47], v[46:47]
	v_add_f32_e32 v58, v65, v58
	v_pk_add_f32 v[44:45], v[44:45], v[56:57] op_sel_hi:[1,0] neg_lo:[0,1] neg_hi:[0,1]
	v_add_f32_e32 v58, v66, v58
	v_pk_mul_f32 v[68:69], v[44:45], v[44:45]
	v_add_f32_e32 v58, v67, v58
	v_pk_add_f32 v[42:43], v[42:43], v[56:57] op_sel_hi:[1,0] neg_lo:[0,1] neg_hi:[0,1]
	v_add_f32_e32 v58, v68, v58
	v_pk_mul_f32 v[70:71], v[42:43], v[42:43]
	v_add_f32_e32 v58, v69, v58
	v_pk_add_f32 v[40:41], v[40:41], v[56:57] op_sel_hi:[1,0] neg_lo:[0,1] neg_hi:[0,1]
	v_add_f32_e32 v58, v70, v58
	v_pk_mul_f32 v[56:57], v[40:41], v[40:41]
	v_add_f32_e32 v58, v71, v58
	v_add_f32_e32 v56, v56, v58
	v_add_f32_e32 v56, v57, v56
	ds_bpermute_b32 v57, v2, v56
	s_waitcnt lgkmcnt(0)
	v_add_f32_e32 v56, v56, v57
	ds_bpermute_b32 v57, v1, v56
	s_waitcnt lgkmcnt(0)
	v_add_f32_e32 v56, v56, v57
	ds_bpermute_b32 v57, v74, v56
	s_waitcnt lgkmcnt(0)
	v_add_f32_e32 v56, v56, v57
	ds_bpermute_b32 v57, v75, v56
	s_waitcnt lgkmcnt(0)
	v_add_f32_e32 v56, v56, v57
	ds_bpermute_b32 v57, v126, v56
	s_waitcnt lgkmcnt(0)
	v_add_f32_e32 v56, v56, v57
	ds_bpermute_b32 v57, v127, v56
	s_waitcnt lgkmcnt(0)
	v_add_f32_e32 v56, v56, v57
	v_fmamk_f32 v56, v56, 0x3a800000, v204
	v_mul_f32_e32 v57, 0x4b800000, v56
	v_cmp_gt_f32_e32 vcc, s22, v56
	s_nop 1
	v_cndmask_b32_e32 v56, v56, v57, vcc
	v_rsq_f32_e32 v56, v56
	s_nop 0
	v_mul_f32_e32 v57, 0x45800000, v56
	v_cndmask_b32_e32 v56, v56, v57, vcc
	v_pk_mul_f32 v[54:55], v[54:55], v[56:57] op_sel_hi:[1,0]
	v_pk_mul_f32 v[52:53], v[52:53], v[56:57] op_sel_hi:[1,0]
	s_waitcnt lgkmcnt(0)
	s_waitcnt vmcnt(0)
	v_pk_fma_f32 v[4:5], v[4:5], v[54:55], v[36:37]
	v_pk_mul_f32 v[36:37], v[50:51], v[56:57] op_sel_hi:[1,0]
	v_pk_fma_f32 v[6:7], v[6:7], v[52:53], v[38:39]
	v_pk_fma_f32 v[8:9], v[8:9], v[36:37], v[32:33]
	v_pk_mul_f32 v[32:33], v[48:49], v[56:57] op_sel_hi:[1,0]
	s_and_b64 vcc, exec, s[0:1]
	v_pk_fma_f32 v[10:11], v[10:11], v[32:33], v[34:35]
	v_pk_mul_f32 v[32:33], v[46:47], v[56:57] op_sel_hi:[1,0]
	s_nop 0
	v_pk_fma_f32 v[12:13], v[12:13], v[32:33], v[28:29]
	v_pk_mul_f32 v[28:29], v[44:45], v[56:57] op_sel_hi:[1,0]
	s_nop 0
	v_pk_fma_f32 v[14:15], v[14:15], v[28:29], v[30:31]
	v_pk_mul_f32 v[28:29], v[42:43], v[56:57] op_sel_hi:[1,0]
	s_nop 0
	v_pk_fma_f32 v[16:17], v[16:17], v[28:29], v[24:25]
	v_pk_mul_f32 v[24:25], v[40:41], v[56:57] op_sel_hi:[1,0]
	s_nop 0
	v_pk_fma_f32 v[18:19], v[18:19], v[24:25], v[26:27]
	global_store_dwordx4 v[22:23], v[4:7], off
	global_store_dwordx4 v[22:23], v[8:11], off offset:16
	global_store_dwordx4 v[22:23], v[12:15], off offset:32
	global_store_dwordx4 v[22:23], v[16:19], off offset:48
	s_cbranch_vccz .LBB0_977
	s_lshl_b64 s[0:1], s[96:97], 10
	s_mul_hi_i32 s3, s2, 0x6000
	s_mulk_i32 s2, 0x6000
	s_add_u32 s2, s70, s2
	s_addc_u32 s3, s71, s3
	v_lshl_add_u64 v[50:51], v[20:21], 2, s[2:3]
	s_mov_b64 s[2:3], 0x19000
	v_add_co_u32_e32 v34, vcc, s86, v50
	v_lshl_add_u64 v[30:31], v[50:51], 0, s[2:3]
	s_mov_b64 s[2:3], 0x18000
	v_addc_co_u32_e32 v35, vcc, 0, v51, vcc
	v_lshl_add_u64 v[46:47], v[50:51], 0, s[2:3]
	v_add_co_u32_e32 v50, vcc, s67, v50
	global_load_dwordx4 v[22:25], v[30:31], off offset:32
	global_load_dwordx4 v[26:29], v[30:31], off offset:16
	v_addc_co_u32_e32 v51, vcc, 0, v51, vcc
	global_load_dwordx4 v[30:33], v[30:31], off offset:48
	s_nop 0
	global_load_dwordx4 v[34:37], v[34:35], off
	s_nop 0
	global_load_dwordx4 v[38:41], v[46:47], off offset:16
	global_load_dwordx4 v[42:45], v[46:47], off offset:48
	s_nop 0
	global_load_dwordx4 v[46:49], v[46:47], off offset:32
	s_lshl_b64 s[0:1], s[0:1], 1
	global_load_dwordx4 v[50:53], v[50:51], off
	s_add_u32 s0, s76, s0
	s_addc_u32 s1, s77, s1
	v_lshl_add_u64 v[20:21], v[20:21], 1, s[0:1]
	s_waitcnt lgkmcnt(0)
	s_waitcnt vmcnt(7)
	v_pk_add_f32 v[22:23], v[22:23], 1.0 op_sel_hi:[1,0]
	s_waitcnt lgkmcnt(0)
	s_waitcnt vmcnt(6)
	v_pk_add_f32 v[26:27], v[26:27], 1.0 op_sel_hi:[1,0]
	v_pk_add_f32 v[28:29], v[28:29], 1.0 op_sel_hi:[1,0]
	s_waitcnt lgkmcnt(0)
	s_waitcnt vmcnt(4)
	v_pk_add_f32 v[34:35], v[34:35], 1.0 op_sel_hi:[1,0]
	v_pk_add_f32 v[36:37], v[36:37], 1.0 op_sel_hi:[1,0]
	v_pk_add_f32 v[24:25], v[24:25], 1.0 op_sel_hi:[1,0]
	v_pk_add_f32 v[30:31], v[30:31], 1.0 op_sel_hi:[1,0]
	v_pk_add_f32 v[32:33], v[32:33], 1.0 op_sel_hi:[1,0]
	s_waitcnt lgkmcnt(0)
	s_waitcnt vmcnt(3)
	v_pk_fma_f32 v[8:9], v[8:9], v[26:27], v[38:39]
	v_pk_fma_f32 v[10:11], v[10:11], v[28:29], v[40:41]
	s_waitcnt lgkmcnt(0)
	s_waitcnt vmcnt(1)
	v_pk_fma_f32 v[12:13], v[12:13], v[22:23], v[46:47]
	s_waitcnt lgkmcnt(0)
	s_waitcnt vmcnt(0)
	v_pk_fma_f32 v[4:5], v[4:5], v[34:35], v[50:51]
	v_pk_fma_f32 v[22:23], v[6:7], v[36:37], v[52:53]
	v_pk_fma_f32 v[14:15], v[14:15], v[24:25], v[48:49]
	v_pk_fma_f32 v[16:17], v[16:17], v[30:31], v[42:43]
	v_pk_fma_f32 v[18:19], v[18:19], v[32:33], v[44:45]
	v_cvt_pk_bf16_f32 v6, v8, v9
	v_cvt_pk_bf16_f32 v7, v10, v11
	v_cvt_pk_bf16_f32 v4, v4, v5
	v_cvt_pk_bf16_f32 v5, v22, v23
	v_cvt_pk_bf16_f32 v8, v12, v13
	v_cvt_pk_bf16_f32 v9, v14, v15
	v_cvt_pk_bf16_f32 v10, v16, v17
	v_cvt_pk_bf16_f32 v11, v18, v19
	global_store_dwordx4 v[20:21], v[4:7], off
	global_store_dwordx4 v[20:21], v[8:11], off offset:16
.LBB0_977:
	s_or_b32 s22, s96, 1
	s_add_i32 s0, s22, s35
	s_ashr_i32 s1, s0, 31
	s_lshr_b32 s1, s1, 19
	s_add_i32 s0, s0, s1
	s_ashr_i32 s2, s0, 13
	s_ashr_i32 s0, s2, 31
	s_add_u32 s1, s2, s87
	s_addc_u32 s0, s0, 0
	s_mulk_i32 s0, 0x6000
	s_mul_hi_u32 s3, s1, 0x6000
	v_mov_b32_e32 v4, v179
	s_add_i32 s3, s3, s0
	s_mulk_i32 s1, 0x6000
	s_add_u32 s0, s70, s1
	v_lshlrev_b32_e32 v20, 4, v4
	s_addc_u32 s1, s71, s3
	s_ashr_i32 s23, s22, 31
	v_readlane_b32 s36, v253, 60
	v_ashrrev_i32_e32 v21, 31, v20
	s_lshl_b64 s[26:27], s[22:23], 12
	v_readlane_b32 s38, v253, 62
	v_lshlrev_b64 v[4:5], 2, v[20:21]
	v_readlane_b32 s39, v253, 63
	s_add_u32 s6, s38, s26
	v_lshl_add_u64 v[22:23], s[0:1], 0, v[4:5]
	s_mov_b64 s[0:1], 0x5000
	s_addc_u32 s7, s39, s27
	v_lshl_add_u64 v[14:15], v[22:23], 0, s[0:1]
	s_lshl_b64 s[0:1], s[22:23], 3
	v_add_co_u32_e32 v22, vcc, s18, v22
	s_add_u32 s0, s64, s0
	s_nop 0
	v_addc_co_u32_e32 v23, vcc, 0, v23, vcc
	v_lshl_add_u64 v[18:19], s[6:7], 0, v[4:5]
	s_addc_u32 s1, s65, s1
	global_load_dwordx4 v[6:9], v[14:15], off offset:48
	global_load_dwordx4 v[10:13], v[14:15], off offset:32
	s_nop 0
	global_load_dwordx4 v[14:17], v[14:15], off offset:16
	s_nop 0
	global_load_dwordx4 v[22:25], v[22:23], off
	s_nop 0
	global_load_dwordx2 v[128:129], v3, s[0:1]
	global_load_dwordx4 v[26:29], v[18:19], off
	global_load_dwordx4 v[30:33], v[18:19], off offset:16
	global_load_dwordx4 v[34:37], v[18:19], off offset:32
	global_load_dwordx4 v[38:41], v[18:19], off offset:48
	v_lshl_add_u64 v[70:71], s[28:29], 0, v[4:5]
	v_lshl_add_u64 v[18:19], s[16:17], 0, v[4:5]
	ds_read_b128 v[42:45], v185 offset:7168
	global_load_dword v184, v187, s[28:29]
	ds_read_b128 v[46:49], v185 offset:3072
	global_load_dword v184, v187, s[16:17]
	ds_read_b128 v[50:53], v185 offset:2048
	global_load_dword v184, v187, s[16:17]
	ds_read_b128 v[54:57], v185 offset:6144
	global_load_dword v184, v187, s[28:29]
	ds_read_b128 v[58:61], v185 offset:5120
	global_load_dword v184, v187, s[28:29]
	ds_read_b128 v[62:65], v185 offset:1024
	global_load_dword v184, v187, s[16:17]
	ds_read_b128 v[66:69], v185 offset:0
	global_load_dword v184, v187, s[16:17]
	s_nop 0
	ds_read_b128 v[70:73], v185 offset:4096
	global_load_dword v184, v187, s[28:29]
	v_readlane_b32 s37, v253, 61
	v_readlane_b32 s36, v255, 42
	v_readlane_b32 s24, v255, 23
	v_readlane_b32 s38, v255, 44
	v_readlane_b32 s25, v255, 24
	s_add_u32 s20, s30, s26
	s_addc_u32 s21, s31, s27
	s_andn2_b64 vcc, exec, s[24:25]
	v_readlane_b32 s40, v254, 0
	v_readlane_b32 s41, v254, 1
	v_readlane_b32 s42, v254, 2
	v_readlane_b32 s43, v254, 3
	v_readlane_b32 s44, v254, 4
	v_readlane_b32 s45, v254, 5
	v_readlane_b32 s46, v254, 6
	v_readlane_b32 s47, v254, 7
	v_readlane_b32 s48, v254, 8
	v_readlane_b32 s49, v254, 9
	v_readlane_b32 s50, v254, 10
	v_readlane_b32 s51, v254, 11
	v_readlane_b32 s37, v255, 43
	v_readlane_b32 s39, v255, 45
	s_waitcnt lgkmcnt(0)
	s_waitcnt vmcnt(13)
	v_pk_add_f32 v[18:19], v[24:25], 1.0 op_sel_hi:[1,0]
	v_pk_add_f32 v[22:23], v[22:23], 1.0 op_sel_hi:[1,0]
	s_waitcnt lgkmcnt(0)
	s_waitcnt vmcnt(11)
	v_pk_add_f32 v[24:25], v[26:27], v[128:129] op_sel_hi:[1,0] neg_lo:[0,1] neg_hi:[0,1]
	v_pk_add_f32 v[26:27], v[28:29], v[128:129] op_sel_hi:[1,0] neg_lo:[0,1] neg_hi:[0,1]
	s_waitcnt lgkmcnt(0)
	s_waitcnt vmcnt(10)
	v_pk_add_f32 v[28:29], v[30:31], v[128:129] op_sel_hi:[1,0] neg_lo:[0,1] neg_hi:[0,1]
	v_pk_add_f32 v[30:31], v[32:33], v[128:129] op_sel_hi:[1,0] neg_lo:[0,1] neg_hi:[0,1]
	s_waitcnt lgkmcnt(0)
	s_waitcnt vmcnt(9)
	v_pk_add_f32 v[32:33], v[34:35], v[128:129] op_sel_hi:[1,0] neg_lo:[0,1] neg_hi:[0,1]
	v_pk_add_f32 v[34:35], v[36:37], v[128:129] op_sel_hi:[1,0] neg_lo:[0,1] neg_hi:[0,1]
	s_waitcnt lgkmcnt(0)
	s_waitcnt vmcnt(8)
	v_pk_add_f32 v[36:37], v[38:39], v[128:129] op_sel_hi:[1,0] neg_lo:[0,1] neg_hi:[0,1]
	v_pk_add_f32 v[38:39], v[40:41], v[128:129] op_sel_hi:[1,0] neg_lo:[0,1] neg_hi:[0,1]
	v_pk_mul_f32 v[24:25], v[128:129], v[24:25] op_sel:[1,0]
	v_pk_mul_f32 v[38:39], v[128:129], v[38:39] op_sel:[1,0]
	s_waitcnt lgkmcnt(0)
	s_waitcnt vmcnt(0)
	v_pk_fma_f32 v[24:25], v[66:67], v[24:25], v[70:71]
	v_pk_mul_f32 v[32:33], v[128:129], v[32:33] op_sel:[1,0]
	v_pk_mul_f32 v[26:27], v[128:129], v[26:27] op_sel:[1,0]
	v_pk_fma_f32 v[38:39], v[38:39], v[48:49], v[44:45]
	v_pk_mul_f32 v[24:25], v[24:25], s[34:35] op_sel_hi:[1,0]
	v_pk_add_f32 v[8:9], v[8:9], 1.0 op_sel_hi:[1,0]
	v_pk_mul_f32 v[36:37], v[128:129], v[36:37] op_sel:[1,0]
	v_pk_fma_f32 v[32:33], v[32:33], v[50:51], v[54:55]
	v_pk_fma_f32 v[26:27], v[26:27], v[68:69], v[72:73]
	v_pk_mul_f32 v[38:39], v[38:39], s[34:35] op_sel_hi:[1,0]
	v_pk_fma_f32 v[54:55], v[110:111], v[22:23], v[24:25]
	v_pk_mul_f32 v[34:35], v[128:129], v[34:35] op_sel:[1,0]
	v_pk_mul_f32 v[28:29], v[128:129], v[28:29] op_sel:[1,0]
	v_pk_fma_f32 v[36:37], v[36:37], v[46:47], v[42:43]
	v_pk_mul_f32 v[26:27], v[26:27], s[34:35] op_sel_hi:[1,0]
	v_pk_fma_f32 v[42:43], v[124:125], v[8:9], v[38:39]
	v_add_f32_e32 v8, 0, v54
	v_pk_fma_f32 v[34:35], v[34:35], v[52:53], v[56:57]
	v_pk_fma_f32 v[28:29], v[28:29], v[62:63], v[58:59]
	v_pk_fma_f32 v[52:53], v[112:113], v[18:19], v[26:27]
	v_add_f32_e32 v8, v8, v55
	v_pk_add_f32 v[14:15], v[14:15], 1.0 op_sel_hi:[1,0]
	v_pk_mul_f32 v[30:31], v[128:129], v[30:31] op_sel:[1,0]
	v_pk_mul_f32 v[28:29], v[28:29], s[34:35] op_sel_hi:[1,0]
	v_add_f32_e32 v8, v8, v52
	v_pk_fma_f32 v[30:31], v[30:31], v[64:65], v[60:61]
	v_pk_fma_f32 v[50:51], v[114:115], v[14:15], v[28:29]
	v_add_f32_e32 v8, v8, v53
	v_pk_add_f32 v[16:17], v[16:17], 1.0 op_sel_hi:[1,0]
	v_pk_mul_f32 v[30:31], v[30:31], s[34:35] op_sel_hi:[1,0]
	v_add_f32_e32 v8, v8, v50
	v_pk_fma_f32 v[48:49], v[116:117], v[16:17], v[30:31]
	v_add_f32_e32 v8, v8, v51
	v_pk_add_f32 v[10:11], v[10:11], 1.0 op_sel_hi:[1,0]
	v_pk_mul_f32 v[32:33], v[32:33], s[34:35] op_sel_hi:[1,0]
	v_add_f32_e32 v8, v8, v48
	v_pk_fma_f32 v[46:47], v[118:119], v[10:11], v[32:33]
	v_add_f32_e32 v8, v8, v49
	v_pk_add_f32 v[12:13], v[12:13], 1.0 op_sel_hi:[1,0]
	v_pk_mul_f32 v[34:35], v[34:35], s[34:35] op_sel_hi:[1,0]
	v_add_f32_e32 v8, v8, v46
	v_pk_fma_f32 v[44:45], v[120:121], v[12:13], v[34:35]
	v_add_f32_e32 v8, v8, v47
	v_pk_add_f32 v[6:7], v[6:7], 1.0 op_sel_hi:[1,0]
	v_pk_mul_f32 v[36:37], v[36:37], s[34:35] op_sel_hi:[1,0]
	v_add_f32_e32 v8, v8, v44
	v_pk_fma_f32 v[6:7], v[122:123], v[6:7], v[36:37]
	v_add_f32_e32 v8, v8, v45
	v_add_f32_e32 v8, v8, v6
	v_add_f32_e32 v8, v8, v7
	v_add_f32_e32 v8, v8, v42
	v_add_f32_e32 v8, v8, v43
	ds_bpermute_b32 v9, v2, v8
	v_lshl_add_u64 v[22:23], s[12:13], 0, v[4:5]
	v_lshl_add_u64 v[38:39], s[90:91], 0, v[4:5]
	s_waitcnt lgkmcnt(0)
	v_add_f32_e32 v8, v8, v9
	ds_bpermute_b32 v9, v1, v8
	s_waitcnt lgkmcnt(0)
	v_add_f32_e32 v8, v8, v9
	ds_bpermute_b32 v9, v74, v8
	s_waitcnt lgkmcnt(0)
	v_add_f32_e32 v8, v8, v9
	ds_bpermute_b32 v9, v75, v8
	s_waitcnt lgkmcnt(0)
	v_add_f32_e32 v26, v8, v9
	ds_bpermute_b32 v27, v126, v26
	ds_read_b128 v[8:11], v185 offset:11264
	global_load_dword v184, v187, s[12:13]
	ds_read_b128 v[12:15], v185 offset:10240
	global_load_dword v184, v187, s[12:13]
	ds_read_b128 v[16:19], v185 offset:9216
	global_load_dword v184, v187, s[12:13]
	s_nop 0
	ds_read_b128 v[22:25], v185 offset:8192
	global_load_dword v184, v187, s[12:13]
	s_waitcnt lgkmcnt(0)
	v_add_f32_e32 v56, v26, v27
	ds_read_b128 v[26:29], v185 offset:15360
	global_load_dword v184, v187, s[90:91]
	ds_read_b128 v[30:33], v185 offset:14336
	global_load_dword v184, v187, s[90:91]
	ds_read_b128 v[34:37], v185 offset:13312
	global_load_dword v184, v187, s[90:91]
	s_nop 0
	ds_read_b128 v[38:41], v185 offset:12288
	global_load_dword v184, v187, s[90:91]
	ds_bpermute_b32 v57, v127, v56
	s_waitcnt lgkmcnt(0)
	v_add_f32_e32 v56, v56, v57
	v_mul_f32_e32 v56, 0x3a800000, v56
	v_pk_add_f32 v[54:55], v[54:55], v[56:57] op_sel_hi:[1,0] neg_lo:[0,1] neg_hi:[0,1]
	v_pk_add_f32 v[52:53], v[52:53], v[56:57] op_sel_hi:[1,0] neg_lo:[0,1] neg_hi:[0,1]
	v_pk_add_f32 v[50:51], v[50:51], v[56:57] op_sel_hi:[1,0] neg_lo:[0,1] neg_hi:[0,1]
	v_pk_add_f32 v[48:49], v[48:49], v[56:57] op_sel_hi:[1,0] neg_lo:[0,1] neg_hi:[0,1]
	v_pk_add_f32 v[46:47], v[46:47], v[56:57] op_sel_hi:[1,0] neg_lo:[0,1] neg_hi:[0,1]
	v_pk_add_f32 v[44:45], v[44:45], v[56:57] op_sel_hi:[1,0] neg_lo:[0,1] neg_hi:[0,1]
	v_pk_add_f32 v[6:7], v[6:7], v[56:57] op_sel_hi:[1,0] neg_lo:[0,1] neg_hi:[0,1]
	v_pk_add_f32 v[42:43], v[42:43], v[56:57] op_sel_hi:[1,0] neg_lo:[0,1] neg_hi:[0,1]
	v_pk_mul_f32 v[56:57], v[54:55], v[54:55]
	v_pk_mul_f32 v[58:59], v[52:53], v[52:53]
	v_add_f32_e32 v56, v56, v57
	v_add_f32_e32 v56, v58, v56
	v_pk_mul_f32 v[60:61], v[50:51], v[50:51]
	v_add_f32_e32 v56, v59, v56
	v_add_f32_e32 v56, v60, v56
	v_pk_mul_f32 v[62:63], v[48:49], v[48:49]
	v_add_f32_e32 v56, v61, v56
	v_add_f32_e32 v56, v62, v56
	v_pk_mul_f32 v[64:65], v[46:47], v[46:47]
	v_add_f32_e32 v56, v63, v56
	v_add_f32_e32 v56, v64, v56
	v_pk_mul_f32 v[66:67], v[44:45], v[44:45]
	v_add_f32_e32 v56, v65, v56
	v_add_f32_e32 v56, v66, v56
	v_pk_mul_f32 v[68:69], v[6:7], v[6:7]
	v_add_f32_e32 v56, v67, v56
	v_add_f32_e32 v56, v68, v56
	v_pk_mul_f32 v[70:71], v[42:43], v[42:43]
	v_add_f32_e32 v56, v69, v56
	v_add_f32_e32 v56, v70, v56
	v_add_f32_e32 v56, v71, v56
	ds_bpermute_b32 v57, v2, v56
	v_cndmask_b32_e64 v58, 0, 1, s[24:25]
	v_cmp_ne_u32_e64 s[6:7], 1, v58
	s_waitcnt lgkmcnt(0)
	v_add_f32_e32 v56, v56, v57
	ds_bpermute_b32 v57, v1, v56
	s_waitcnt lgkmcnt(0)
	v_add_f32_e32 v56, v56, v57
	ds_bpermute_b32 v57, v74, v56
	s_waitcnt lgkmcnt(0)
	v_add_f32_e32 v56, v56, v57
	ds_bpermute_b32 v57, v75, v56
	s_waitcnt lgkmcnt(0)
	v_add_f32_e32 v56, v56, v57
	ds_bpermute_b32 v57, v126, v56
	s_waitcnt lgkmcnt(0)
	v_add_f32_e32 v56, v56, v57
	ds_bpermute_b32 v57, v127, v56
	s_waitcnt lgkmcnt(0)
	v_add_f32_e32 v56, v56, v57
	v_fmamk_f32 v56, v56, 0x3a800000, v204
	v_mul_f32_e32 v57, 0x4b800000, v56
	v_cmp_gt_f32_e64 s[0:1], s38, v56
	s_nop 1
	v_cndmask_b32_e64 v56, v56, v57, s[0:1]
	v_rsq_f32_e32 v58, v56
	v_lshl_add_u64 v[56:57], s[20:21], 0, v[4:5]
	v_mul_f32_e32 v4, 0x45800000, v58
	v_cndmask_b32_e64 v4, v58, v4, s[0:1]
	v_pk_mul_f32 v[54:55], v[54:55], v[4:5] op_sel_hi:[1,0]
	v_pk_mul_f32 v[52:53], v[52:53], v[4:5] op_sel_hi:[1,0]
	v_pk_mul_f32 v[50:51], v[50:51], v[4:5] op_sel_hi:[1,0]
	v_pk_mul_f32 v[48:49], v[48:49], v[4:5] op_sel_hi:[1,0]
	v_pk_mul_f32 v[46:47], v[46:47], v[4:5] op_sel_hi:[1,0]
	v_pk_mul_f32 v[44:45], v[44:45], v[4:5] op_sel_hi:[1,0]
	v_pk_mul_f32 v[58:59], v[6:7], v[4:5] op_sel_hi:[1,0]
	v_pk_mul_f32 v[42:43], v[42:43], v[4:5] op_sel_hi:[1,0]
	s_waitcnt lgkmcnt(0)
	s_waitcnt vmcnt(0)
	v_pk_fma_f32 v[4:5], v[22:23], v[54:55], v[38:39]
	v_pk_fma_f32 v[6:7], v[24:25], v[52:53], v[40:41]
	v_pk_fma_f32 v[16:17], v[16:17], v[50:51], v[34:35]
	v_pk_fma_f32 v[18:19], v[18:19], v[48:49], v[36:37]
	v_pk_fma_f32 v[12:13], v[12:13], v[46:47], v[30:31]
	v_pk_fma_f32 v[14:15], v[14:15], v[44:45], v[32:33]
	v_pk_fma_f32 v[8:9], v[8:9], v[58:59], v[26:27]
	v_pk_fma_f32 v[10:11], v[10:11], v[42:43], v[28:29]
	global_store_dwordx4 v[56:57], v[4:7], off
	global_store_dwordx4 v[56:57], v[16:19], off offset:16
	global_store_dwordx4 v[56:57], v[12:15], off offset:32
	global_store_dwordx4 v[56:57], v[8:11], off offset:48
	s_cbranch_vccnz .LBB0_979
	s_lshl_b64 s[0:1], s[22:23], 10
	s_mul_hi_i32 s3, s2, 0x6000
	s_mulk_i32 s2, 0x6000
	s_add_u32 s2, s70, s2
	s_addc_u32 s3, s71, s3
	v_lshl_add_u64 v[50:51], v[20:21], 2, s[2:3]
	s_mov_b64 s[2:3], 0x19000
	v_add_co_u32_e32 v34, vcc, s86, v50
	v_lshl_add_u64 v[30:31], v[50:51], 0, s[2:3]
	s_mov_b64 s[2:3], 0x18000
	v_addc_co_u32_e32 v35, vcc, 0, v51, vcc
	v_lshl_add_u64 v[46:47], v[50:51], 0, s[2:3]
	v_add_co_u32_e32 v50, vcc, s67, v50
	global_load_dwordx4 v[22:25], v[30:31], off offset:32
	global_load_dwordx4 v[26:29], v[30:31], off offset:16
	v_addc_co_u32_e32 v51, vcc, 0, v51, vcc
	global_load_dwordx4 v[30:33], v[30:31], off offset:48
	s_nop 0
	global_load_dwordx4 v[34:37], v[34:35], off
	s_nop 0
	global_load_dwordx4 v[38:41], v[46:47], off offset:16
	global_load_dwordx4 v[42:45], v[46:47], off offset:48
	s_nop 0
	global_load_dwordx4 v[46:49], v[46:47], off offset:32
	s_lshl_b64 s[0:1], s[0:1], 1
	global_load_dwordx4 v[50:53], v[50:51], off
	s_add_u32 s0, s76, s0
	s_addc_u32 s1, s77, s1
	v_lshl_add_u64 v[20:21], v[20:21], 1, s[0:1]
	s_waitcnt lgkmcnt(0)
	s_waitcnt vmcnt(7)
	v_pk_add_f32 v[22:23], v[22:23], 1.0 op_sel_hi:[1,0]
	s_waitcnt lgkmcnt(0)
	s_waitcnt vmcnt(6)
	v_pk_add_f32 v[26:27], v[26:27], 1.0 op_sel_hi:[1,0]
	v_pk_add_f32 v[28:29], v[28:29], 1.0 op_sel_hi:[1,0]
	s_waitcnt lgkmcnt(0)
	s_waitcnt vmcnt(4)
	v_pk_add_f32 v[34:35], v[34:35], 1.0 op_sel_hi:[1,0]
	v_pk_add_f32 v[36:37], v[36:37], 1.0 op_sel_hi:[1,0]
	v_pk_add_f32 v[24:25], v[24:25], 1.0 op_sel_hi:[1,0]
	v_pk_add_f32 v[30:31], v[30:31], 1.0 op_sel_hi:[1,0]
	v_pk_add_f32 v[32:33], v[32:33], 1.0 op_sel_hi:[1,0]
	s_waitcnt lgkmcnt(0)
	s_waitcnt vmcnt(3)
	v_pk_fma_f32 v[16:17], v[16:17], v[26:27], v[38:39]
	v_pk_fma_f32 v[18:19], v[18:19], v[28:29], v[40:41]
	s_waitcnt lgkmcnt(0)
	s_waitcnt vmcnt(0)
	v_pk_fma_f32 v[4:5], v[4:5], v[34:35], v[50:51]
	v_pk_fma_f32 v[26:27], v[6:7], v[36:37], v[52:53]
	v_pk_fma_f32 v[12:13], v[12:13], v[22:23], v[46:47]
	v_pk_fma_f32 v[14:15], v[14:15], v[24:25], v[48:49]
	v_pk_fma_f32 v[22:23], v[8:9], v[30:31], v[42:43]
	v_pk_fma_f32 v[24:25], v[10:11], v[32:33], v[44:45]
	v_cvt_pk_bf16_f32 v6, v16, v17
	v_cvt_pk_bf16_f32 v7, v18, v19
	v_cvt_pk_bf16_f32 v4, v4, v5
	v_cvt_pk_bf16_f32 v5, v26, v27
	v_cvt_pk_bf16_f32 v8, v12, v13
	v_cvt_pk_bf16_f32 v9, v14, v15
	v_cvt_pk_bf16_f32 v10, v22, v23
	v_cvt_pk_bf16_f32 v11, v24, v25
	global_store_dwordx4 v[20:21], v[4:7], off
	global_store_dwordx4 v[20:21], v[8:11], off offset:16
.LBB0_979:
	s_or_b32 s0, s96, 2
	s_add_i32 s1, s0, s35
	s_ashr_i32 s2, s1, 31
	s_lshr_b32 s2, s2, 19
	s_add_i32 s1, s1, s2
	s_ashr_i32 s2, s1, 13
	s_ashr_i32 s1, s2, 31
	s_add_u32 s3, s2, s87
	s_addc_u32 s1, s1, 0
	s_mulk_i32 s1, 0x6000
	s_mul_hi_u32 s20, s3, 0x6000
	v_mov_b32_e32 v4, v179
	s_add_i32 s1, s20, s1
	s_mulk_i32 s3, 0x6000
	s_add_u32 s20, s70, s3
	v_lshlrev_b32_e32 v52, 4, v4
	s_addc_u32 s21, s71, s1
	s_ashr_i32 s1, s0, 31
	v_readlane_b32 s36, v253, 60
	v_ashrrev_i32_e32 v53, 31, v52
	s_lshl_b64 s[22:23], s[0:1], 12
	v_readlane_b32 s38, v253, 62
	v_lshlrev_b64 v[54:55], 2, v[52:53]
	v_readlane_b32 s39, v253, 63
	s_add_u32 s24, s38, s22
	v_lshl_add_u64 v[20:21], s[20:21], 0, v[54:55]
	s_mov_b64 s[20:21], 0x5000
	s_addc_u32 s25, s39, s23
	v_lshl_add_u64 v[22:23], v[20:21], 0, s[20:21]
	s_lshl_b64 s[20:21], s[0:1], 3
	s_add_u32 s20, s64, s20
	s_addc_u32 s21, s65, s21
	global_load_dwordx2 v[58:59], v3, s[20:21]
	v_lshl_add_u64 v[16:17], s[24:25], 0, v[54:55]
	global_load_dwordx4 v[4:7], v[16:17], off offset:48
	global_load_dwordx4 v[8:11], v[16:17], off offset:32
	global_load_dwordx4 v[12:15], v[16:17], off offset:16
	s_nop 0
	global_load_dwordx4 v[16:19], v[16:17], off
	v_lshl_add_u64 v[24:25], s[16:17], 0, v[54:55]
	v_lshl_add_u64 v[26:27], s[28:29], 0, v[54:55]
	v_lshl_add_u64 v[32:33], s[90:91], 0, v[54:55]
	v_readlane_b32 s24, v255, 42
	v_readlane_b32 s26, v255, 44
	s_add_u32 s20, s30, s22
	s_addc_u32 s21, s31, s23
	v_readlane_b32 s37, v253, 61
	v_readlane_b32 s40, v254, 0
	v_readlane_b32 s41, v254, 1
	v_readlane_b32 s42, v254, 2
	v_readlane_b32 s43, v254, 3
	v_readlane_b32 s44, v254, 4
	v_readlane_b32 s45, v254, 5
	v_readlane_b32 s46, v254, 6
	v_readlane_b32 s47, v254, 7
	v_readlane_b32 s48, v254, 8
	v_readlane_b32 s49, v254, 9
	v_readlane_b32 s50, v254, 10
	v_readlane_b32 s51, v254, 11
	v_readlane_b32 s25, v255, 43
	v_readlane_b32 s27, v255, 45
	s_waitcnt lgkmcnt(0)
	s_waitcnt vmcnt(3)
	v_pk_add_f32 v[62:63], v[4:5], v[58:59] op_sel_hi:[1,0] neg_lo:[0,1] neg_hi:[0,1]
	v_pk_add_f32 v[4:5], v[6:7], v[58:59] op_sel_hi:[1,0] neg_lo:[0,1] neg_hi:[0,1]
	v_add_co_u32_e32 v6, vcc, s18, v20
	s_waitcnt lgkmcnt(0)
	s_waitcnt vmcnt(1)
	v_pk_add_f32 v[70:71], v[14:15], v[58:59] op_sel_hi:[1,0] neg_lo:[0,1] neg_hi:[0,1]
	v_addc_co_u32_e32 v7, vcc, 0, v21, vcc
	global_load_dwordx4 v[36:39], v[6:7], off
	global_load_dwordx4 v[110:113], v[22:23], off offset:48
	global_load_dwordx4 v[114:117], v[22:23], off offset:32
	global_load_dwordx4 v[44:47], v[22:23], off offset:16
	ds_read_b128 v[118:121], v185 offset:3072
	global_load_dword v184, v187, s[16:17]
	ds_read_b128 v[122:125], v185 offset:2048
	global_load_dword v184, v187, s[16:17]
	ds_read_b128 v[48:51], v185 offset:1024
	global_load_dword v184, v187, s[16:17]
	ds_read_b128 v[40:43], v185 offset:0
	global_load_dword v184, v187, s[16:17]
	ds_read_b128 v[128:131], v185 offset:7168
	global_load_dword v184, v187, s[28:29]
	ds_read_b128 v[132:135], v185 offset:6144
	global_load_dword v184, v187, s[28:29]
	ds_read_b128 v[136:139], v185 offset:5120
	global_load_dword v184, v187, s[28:29]
	ds_read_b128 v[140:143], v185 offset:4096
	global_load_dword v184, v187, s[28:29]
	v_pk_mul_f32 v[70:71], v[58:59], v[70:71] op_sel:[1,0]
	v_pk_add_f32 v[66:67], v[12:13], v[58:59] op_sel_hi:[1,0] neg_lo:[0,1] neg_hi:[0,1]
	s_waitcnt lgkmcnt(0)
	s_waitcnt vmcnt(12)
	v_pk_add_f32 v[64:65], v[18:19], v[58:59] op_sel_hi:[1,0] neg_lo:[0,1] neg_hi:[0,1]
	v_pk_add_f32 v[60:61], v[16:17], v[58:59] op_sel_hi:[1,0] neg_lo:[0,1] neg_hi:[0,1]
	v_pk_mul_f32 v[4:5], v[58:59], v[4:5] op_sel:[1,0]
	v_pk_add_f32 v[68:69], v[10:11], v[58:59] op_sel_hi:[1,0] neg_lo:[0,1] neg_hi:[0,1]
	v_pk_mul_f32 v[62:63], v[58:59], v[62:63] op_sel:[1,0]
	v_pk_add_f32 v[72:73], v[8:9], v[58:59] op_sel_hi:[1,0] neg_lo:[0,1] neg_hi:[0,1]
	v_pk_mul_f32 v[68:69], v[58:59], v[68:69] op_sel:[1,0]
	v_pk_mul_f32 v[72:73], v[58:59], v[72:73] op_sel:[1,0]
	v_lshl_add_u64 v[8:9], s[12:13], 0, v[54:55]
	s_waitcnt lgkmcnt(0)
	s_waitcnt vmcnt(11)
	v_pk_add_f32 v[38:39], v[38:39], 1.0 op_sel_hi:[1,0]
	v_pk_add_f32 v[36:37], v[36:37], 1.0 op_sel_hi:[1,0]
	s_waitcnt lgkmcnt(0)
	s_waitcnt vmcnt(10)
	v_pk_add_f32 v[6:7], v[112:113], 1.0 op_sel_hi:[1,0]
	s_waitcnt lgkmcnt(0)
	s_waitcnt vmcnt(8)
	v_pk_add_f32 v[46:47], v[46:47], 1.0 op_sel_hi:[1,0]
	v_pk_add_f32 v[44:45], v[44:45], 1.0 op_sel_hi:[1,0]
	s_waitcnt lgkmcnt(0)
	s_waitcnt vmcnt(3)
	v_pk_fma_f32 v[4:5], v[4:5], v[120:121], v[130:131]
	s_nop 0
	v_pk_mul_f32 v[4:5], v[4:5], s[34:35] op_sel_hi:[1,0]
	s_waitcnt lgkmcnt(0)
	s_waitcnt vmcnt(1)
	v_pk_fma_f32 v[50:51], v[70:71], v[50:51], v[138:139]
	v_pk_fma_f32 v[62:63], v[62:63], v[118:119], v[128:129]
	v_pk_mul_f32 v[50:51], v[50:51], s[34:35] op_sel_hi:[1,0]
	v_pk_fma_f32 v[56:57], v[108:109], v[6:7], v[4:5]
	v_pk_fma_f32 v[46:47], v[100:101], v[46:47], v[50:51]
	v_pk_mul_f32 v[50:51], v[58:59], v[66:67] op_sel:[1,0]
	v_pk_mul_f32 v[62:63], v[62:63], s[34:35] op_sel_hi:[1,0]
	v_pk_fma_f32 v[48:49], v[50:51], v[48:49], v[136:137]
	v_pk_add_f32 v[108:109], v[110:111], 1.0 op_sel_hi:[1,0]
	v_pk_mul_f32 v[48:49], v[48:49], s[34:35] op_sel_hi:[1,0]
	v_pk_fma_f32 v[68:69], v[68:69], v[124:125], v[134:135]
	v_pk_fma_f32 v[44:45], v[98:99], v[44:45], v[48:49]
	v_pk_mul_f32 v[48:49], v[58:59], v[64:65] op_sel:[1,0]
	v_pk_fma_f32 v[62:63], v[106:107], v[108:109], v[62:63]
	s_waitcnt lgkmcnt(0)
	s_waitcnt vmcnt(0)
	v_pk_fma_f32 v[42:43], v[48:49], v[42:43], v[142:143]
	v_pk_mul_f32 v[68:69], v[68:69], s[34:35] op_sel_hi:[1,0]
	v_pk_mul_f32 v[42:43], v[42:43], s[34:35] op_sel_hi:[1,0]
	v_pk_add_f32 v[106:107], v[116:117], 1.0 op_sel_hi:[1,0]
	v_pk_fma_f32 v[38:39], v[96:97], v[38:39], v[42:43]
	v_pk_mul_f32 v[42:43], v[58:59], v[60:61] op_sel:[1,0]
	v_pk_fma_f32 v[72:73], v[72:73], v[122:123], v[132:133]
	v_pk_fma_f32 v[40:41], v[40:41], v[42:43], v[140:141]
	v_pk_fma_f32 v[68:69], v[104:105], v[106:107], v[68:69]
	v_pk_mul_f32 v[40:41], v[40:41], s[34:35] op_sel_hi:[1,0]
	v_pk_mul_f32 v[72:73], v[72:73], s[34:35] op_sel_hi:[1,0]
	v_pk_fma_f32 v[36:37], v[94:95], v[36:37], v[40:41]
	v_pk_add_f32 v[104:105], v[114:115], 1.0 op_sel_hi:[1,0]
	v_add_f32_e32 v40, 0, v36
	v_add_f32_e32 v40, v40, v37
	v_add_f32_e32 v40, v40, v38
	v_add_f32_e32 v40, v40, v39
	v_add_f32_e32 v40, v40, v44
	v_add_f32_e32 v40, v40, v45
	v_add_f32_e32 v40, v40, v46
	v_pk_fma_f32 v[72:73], v[102:103], v[104:105], v[72:73]
	v_add_f32_e32 v40, v40, v47
	v_add_f32_e32 v40, v40, v72
	v_add_f32_e32 v40, v40, v73
	v_add_f32_e32 v40, v40, v68
	v_add_f32_e32 v40, v40, v69
	v_add_f32_e32 v40, v40, v62
	v_add_f32_e32 v40, v40, v63
	v_add_f32_e32 v40, v40, v56
	v_add_f32_e32 v40, v40, v57
	ds_bpermute_b32 v41, v2, v40
	ds_read_b128 v[4:7], v185 offset:11264
	global_load_dword v184, v187, s[12:13]
	ds_read_b128 v[12:15], v185 offset:10240
	global_load_dword v184, v187, s[12:13]
	ds_read_b128 v[20:23], v185 offset:9216
	global_load_dword v184, v187, s[12:13]
	ds_read_b128 v[28:31], v185 offset:8192
	global_load_dword v184, v187, s[12:13]
	s_nop 0
	ds_read_b128 v[8:11], v185 offset:15360
	global_load_dword v184, v187, s[90:91]
	ds_read_b128 v[16:19], v185 offset:14336
	global_load_dword v184, v187, s[90:91]
	ds_read_b128 v[24:27], v185 offset:13312
	global_load_dword v184, v187, s[90:91]
	s_nop 0
	ds_read_b128 v[32:35], v185 offset:12288
	global_load_dword v184, v187, s[90:91]
	s_waitcnt lgkmcnt(0)
	v_add_f32_e32 v40, v40, v41
	ds_bpermute_b32 v41, v1, v40
	s_waitcnt lgkmcnt(0)
	v_add_f32_e32 v40, v40, v41
	ds_bpermute_b32 v41, v74, v40
	s_waitcnt lgkmcnt(0)
	v_add_f32_e32 v40, v40, v41
	ds_bpermute_b32 v41, v75, v40
	s_waitcnt lgkmcnt(0)
	v_add_f32_e32 v40, v40, v41
	ds_bpermute_b32 v41, v126, v40
	s_waitcnt lgkmcnt(0)
	v_add_f32_e32 v40, v40, v41
	ds_bpermute_b32 v41, v127, v40
	s_waitcnt lgkmcnt(0)
	v_add_f32_e32 v40, v40, v41
	v_mul_f32_e32 v40, 0x3a800000, v40
	v_pk_add_f32 v[36:37], v[36:37], v[40:41] op_sel_hi:[1,0] neg_lo:[0,1] neg_hi:[0,1]
	v_pk_add_f32 v[38:39], v[38:39], v[40:41] op_sel_hi:[1,0] neg_lo:[0,1] neg_hi:[0,1]
	v_pk_mul_f32 v[42:43], v[36:37], v[36:37]
	v_pk_mul_f32 v[48:49], v[38:39], v[38:39]
	v_add_f32_e32 v42, v42, v43
	v_pk_add_f32 v[44:45], v[44:45], v[40:41] op_sel_hi:[1,0] neg_lo:[0,1] neg_hi:[0,1]
	v_add_f32_e32 v42, v48, v42
	v_pk_mul_f32 v[50:51], v[44:45], v[44:45]
	v_add_f32_e32 v42, v49, v42
	v_pk_add_f32 v[46:47], v[46:47], v[40:41] op_sel_hi:[1,0] neg_lo:[0,1] neg_hi:[0,1]
	v_add_f32_e32 v42, v50, v42
	v_pk_mul_f32 v[58:59], v[46:47], v[46:47]
	v_add_f32_e32 v42, v51, v42
	v_pk_add_f32 v[60:61], v[72:73], v[40:41] op_sel_hi:[1,0] neg_lo:[0,1] neg_hi:[0,1]
	v_add_f32_e32 v42, v58, v42
	v_pk_mul_f32 v[64:65], v[60:61], v[60:61]
	v_add_f32_e32 v42, v59, v42
	v_pk_add_f32 v[66:67], v[68:69], v[40:41] op_sel_hi:[1,0] neg_lo:[0,1] neg_hi:[0,1]
	v_add_f32_e32 v42, v64, v42
	v_pk_mul_f32 v[68:69], v[66:67], v[66:67]
	v_add_f32_e32 v42, v65, v42
	v_pk_add_f32 v[62:63], v[62:63], v[40:41] op_sel_hi:[1,0] neg_lo:[0,1] neg_hi:[0,1]
	v_add_f32_e32 v42, v68, v42
	v_pk_mul_f32 v[70:71], v[62:63], v[62:63]
	v_add_f32_e32 v42, v69, v42
	v_pk_add_f32 v[40:41], v[56:57], v[40:41] op_sel_hi:[1,0] neg_lo:[0,1] neg_hi:[0,1]
	v_add_f32_e32 v42, v70, v42
	v_pk_mul_f32 v[56:57], v[40:41], v[40:41]
	v_add_f32_e32 v42, v71, v42
	v_add_f32_e32 v42, v56, v42
	v_add_f32_e32 v42, v57, v42
	ds_bpermute_b32 v43, v2, v42
	s_waitcnt lgkmcnt(0)
	v_add_f32_e32 v42, v42, v43
	ds_bpermute_b32 v43, v1, v42
	s_waitcnt lgkmcnt(0)
	v_add_f32_e32 v42, v42, v43
	ds_bpermute_b32 v43, v74, v42
	s_waitcnt lgkmcnt(0)
	v_add_f32_e32 v42, v42, v43
	ds_bpermute_b32 v43, v75, v42
	s_waitcnt lgkmcnt(0)
	v_add_f32_e32 v42, v42, v43
	ds_bpermute_b32 v43, v126, v42
	s_waitcnt lgkmcnt(0)
	v_add_f32_e32 v42, v42, v43
	ds_bpermute_b32 v43, v127, v42
	s_waitcnt lgkmcnt(0)
	v_add_f32_e32 v42, v42, v43
	v_fmamk_f32 v42, v42, 0x3a800000, v204
	v_cmp_gt_f32_e32 vcc, s26, v42
	v_mul_f32_e32 v43, 0x4b800000, v42
	s_nop 0
	v_cndmask_b32_e32 v42, v42, v43, vcc
	v_rsq_f32_e32 v42, v42
	s_nop 0
	v_mul_f32_e32 v43, 0x45800000, v42
	v_cndmask_b32_e32 v42, v42, v43, vcc
	v_pk_mul_f32 v[36:37], v[36:37], v[42:43] op_sel_hi:[1,0]
	s_and_b64 vcc, exec, s[6:7]
	s_waitcnt lgkmcnt(0)
	s_waitcnt vmcnt(0)
	v_pk_fma_f32 v[28:29], v[28:29], v[36:37], v[32:33]
	v_pk_mul_f32 v[32:33], v[38:39], v[42:43] op_sel_hi:[1,0]
	s_nop 0
	v_pk_fma_f32 v[30:31], v[30:31], v[32:33], v[34:35]
	v_pk_mul_f32 v[32:33], v[44:45], v[42:43] op_sel_hi:[1,0]
	s_nop 0
	v_pk_fma_f32 v[20:21], v[20:21], v[32:33], v[24:25]
	v_pk_mul_f32 v[24:25], v[46:47], v[42:43] op_sel_hi:[1,0]
	s_nop 0
	v_pk_fma_f32 v[22:23], v[22:23], v[24:25], v[26:27]
	v_pk_mul_f32 v[24:25], v[60:61], v[42:43] op_sel_hi:[1,0]
	s_nop 0
	v_pk_fma_f32 v[12:13], v[12:13], v[24:25], v[16:17]
	v_pk_mul_f32 v[16:17], v[66:67], v[42:43] op_sel_hi:[1,0]
	s_nop 0
	v_pk_fma_f32 v[14:15], v[14:15], v[16:17], v[18:19]
	v_pk_mul_f32 v[16:17], v[62:63], v[42:43] op_sel_hi:[1,0]
	s_nop 0
	v_pk_fma_f32 v[4:5], v[4:5], v[16:17], v[8:9]
	v_pk_mul_f32 v[8:9], v[40:41], v[42:43] op_sel_hi:[1,0]
	s_nop 0
	v_pk_fma_f32 v[6:7], v[6:7], v[8:9], v[10:11]
	v_lshl_add_u64 v[8:9], s[20:21], 0, v[54:55]
	global_store_dwordx4 v[8:9], v[28:31], off
	global_store_dwordx4 v[8:9], v[20:23], off offset:16
	global_store_dwordx4 v[8:9], v[12:15], off offset:32
	global_store_dwordx4 v[8:9], v[4:7], off offset:48
	s_cbranch_vccnz .LBB0_981
	s_lshl_b64 s[0:1], s[0:1], 10
	s_mul_hi_i32 s3, s2, 0x6000
	s_mulk_i32 s2, 0x6000
	s_add_u32 s2, s70, s2
	s_addc_u32 s3, s71, s3
	v_lshl_add_u64 v[48:49], v[52:53], 2, s[2:3]
	s_mov_b64 s[2:3], 0x19000
	v_add_co_u32_e32 v32, vcc, s86, v48
	v_lshl_add_u64 v[24:25], v[48:49], 0, s[2:3]
	s_mov_b64 s[2:3], 0x18000
	v_addc_co_u32_e32 v33, vcc, 0, v49, vcc
	v_lshl_add_u64 v[44:45], v[48:49], 0, s[2:3]
	v_add_co_u32_e32 v48, vcc, s67, v48
	global_load_dwordx4 v[8:11], v[24:25], off offset:32
	global_load_dwordx4 v[16:19], v[24:25], off offset:16
	v_addc_co_u32_e32 v49, vcc, 0, v49, vcc
	global_load_dwordx4 v[24:27], v[24:25], off offset:48
	s_nop 0
	global_load_dwordx4 v[32:35], v[32:33], off
	s_nop 0
	global_load_dwordx4 v[36:39], v[44:45], off offset:16
	global_load_dwordx4 v[40:43], v[44:45], off offset:48
	s_nop 0
	global_load_dwordx4 v[44:47], v[44:45], off offset:32
	s_lshl_b64 s[0:1], s[0:1], 1
	global_load_dwordx4 v[48:51], v[48:49], off
	s_add_u32 s0, s76, s0
	s_addc_u32 s1, s77, s1
	v_lshl_add_u64 v[52:53], v[52:53], 1, s[0:1]
	s_waitcnt lgkmcnt(0)
	s_waitcnt vmcnt(7)
	v_pk_add_f32 v[8:9], v[8:9], 1.0 op_sel_hi:[1,0]
	s_waitcnt lgkmcnt(0)
	s_waitcnt vmcnt(6)
	v_pk_add_f32 v[16:17], v[16:17], 1.0 op_sel_hi:[1,0]
	v_pk_add_f32 v[18:19], v[18:19], 1.0 op_sel_hi:[1,0]
	v_pk_add_f32 v[10:11], v[10:11], 1.0 op_sel_hi:[1,0]
	s_waitcnt lgkmcnt(0)
	s_waitcnt vmcnt(5)
	v_pk_add_f32 v[24:25], v[24:25], 1.0 op_sel_hi:[1,0]
	s_waitcnt lgkmcnt(0)
	s_waitcnt vmcnt(4)
	v_pk_add_f32 v[32:33], v[32:33], 1.0 op_sel_hi:[1,0]
	v_pk_add_f32 v[34:35], v[34:35], 1.0 op_sel_hi:[1,0]
	v_pk_add_f32 v[26:27], v[26:27], 1.0 op_sel_hi:[1,0]
	s_waitcnt lgkmcnt(0)
	s_waitcnt vmcnt(3)
	v_pk_fma_f32 v[16:17], v[20:21], v[16:17], v[36:37]
	v_pk_fma_f32 v[18:19], v[22:23], v[18:19], v[38:39]
	s_waitcnt lgkmcnt(0)
	s_waitcnt vmcnt(1)
	v_pk_fma_f32 v[8:9], v[12:13], v[8:9], v[44:45]
	v_pk_fma_f32 v[10:11], v[14:15], v[10:11], v[46:47]
	v_pk_fma_f32 v[4:5], v[4:5], v[24:25], v[40:41]
	s_waitcnt lgkmcnt(0)
	s_waitcnt vmcnt(0)
	v_pk_fma_f32 v[14:15], v[28:29], v[32:33], v[48:49]
	v_pk_fma_f32 v[20:21], v[30:31], v[34:35], v[50:51]
	v_pk_fma_f32 v[12:13], v[6:7], v[26:27], v[42:43]
	v_cvt_pk_bf16_f32 v6, v16, v17
	v_cvt_pk_bf16_f32 v7, v18, v19
	v_cvt_pk_bf16_f32 v8, v8, v9
	v_cvt_pk_bf16_f32 v9, v10, v11
	v_cvt_pk_bf16_f32 v10, v4, v5
	v_cvt_pk_bf16_f32 v4, v14, v15
	v_cvt_pk_bf16_f32 v5, v20, v21
	v_cvt_pk_bf16_f32 v11, v12, v13
	global_store_dwordx4 v[52:53], v[4:7], off
	global_store_dwordx4 v[52:53], v[8:11], off offset:16
.LBB0_981:
	s_or_b32 s22, s96, 3
	s_add_i32 s0, s22, s35
	s_ashr_i32 s1, s0, 31
	s_lshr_b32 s1, s1, 19
	s_add_i32 s0, s0, s1
	s_ashr_i32 s2, s0, 13
	s_ashr_i32 s0, s2, 31
	s_add_u32 s1, s2, s87
	s_addc_u32 s0, s0, 0
	s_mulk_i32 s0, 0x6000
	s_mul_hi_u32 s3, s1, 0x6000
	v_mov_b32_e32 v4, v179
	s_add_i32 s3, s3, s0
	s_mulk_i32 s1, 0x6000
	s_add_u32 s0, s70, s1
	v_lshlrev_b32_e32 v20, 4, v4
	s_addc_u32 s1, s71, s3
	s_ashr_i32 s23, s22, 31
	v_readlane_b32 s36, v253, 60
	v_ashrrev_i32_e32 v21, 31, v20
	s_lshl_b64 s[26:27], s[22:23], 12
	v_readlane_b32 s38, v253, 62
	v_lshlrev_b64 v[4:5], 2, v[20:21]
	v_readlane_b32 s39, v253, 63
	s_add_u32 s20, s38, s26
	v_lshl_add_u64 v[22:23], s[0:1], 0, v[4:5]
	s_mov_b64 s[0:1], 0x5000
	s_addc_u32 s21, s39, s27
	v_lshl_add_u64 v[14:15], v[22:23], 0, s[0:1]
	s_lshl_b64 s[0:1], s[22:23], 3
	v_add_co_u32_e32 v22, vcc, s18, v22
	s_add_u32 s0, s64, s0
	s_nop 0
	v_addc_co_u32_e32 v23, vcc, 0, v23, vcc
	v_lshl_add_u64 v[18:19], s[20:21], 0, v[4:5]
	s_addc_u32 s1, s65, s1
	global_load_dwordx4 v[6:9], v[14:15], off offset:48
	global_load_dwordx4 v[10:13], v[14:15], off offset:32
	s_nop 0
	global_load_dwordx4 v[14:17], v[14:15], off offset:16
	s_nop 0
	global_load_dwordx4 v[22:25], v[22:23], off
	s_nop 0
	global_load_dwordx2 v[94:95], v3, s[0:1]
	global_load_dwordx4 v[26:29], v[18:19], off
	global_load_dwordx4 v[30:33], v[18:19], off offset:16
	global_load_dwordx4 v[34:37], v[18:19], off offset:32
	global_load_dwordx4 v[38:41], v[18:19], off offset:48
	v_lshl_add_u64 v[70:71], s[28:29], 0, v[4:5]
	v_lshl_add_u64 v[18:19], s[16:17], 0, v[4:5]
	ds_read_b128 v[42:45], v185 offset:7168
	global_load_dword v184, v187, s[28:29]
	ds_read_b128 v[46:49], v185 offset:3072
	global_load_dword v184, v187, s[16:17]
	ds_read_b128 v[50:53], v185 offset:2048
	global_load_dword v184, v187, s[16:17]
	ds_read_b128 v[54:57], v185 offset:6144
	global_load_dword v184, v187, s[28:29]
	ds_read_b128 v[58:61], v185 offset:5120
	global_load_dword v184, v187, s[28:29]
	ds_read_b128 v[62:65], v185 offset:1024
	global_load_dword v184, v187, s[16:17]
	ds_read_b128 v[66:69], v185 offset:0
	global_load_dword v184, v187, s[16:17]
	s_nop 0
	ds_read_b128 v[70:73], v185 offset:4096
	global_load_dword v184, v187, s[28:29]
	v_readlane_b32 s40, v254, 0
	v_readlane_b32 s41, v254, 1
	v_readlane_b32 s42, v254, 2
	v_readlane_b32 s43, v254, 3
	v_readlane_b32 s40, v255, 42
	v_readlane_b32 s42, v255, 44
	s_add_u32 s20, s30, s26
	s_addc_u32 s21, s31, s27
	v_readlane_b32 s43, v255, 45
	s_and_b64 vcc, exec, s[6:7]
	v_readlane_b32 s37, v253, 61
	v_readlane_b32 s44, v254, 4
	v_readlane_b32 s45, v254, 5
	v_readlane_b32 s46, v254, 6
	v_readlane_b32 s47, v254, 7
	v_readlane_b32 s48, v254, 8
	v_readlane_b32 s49, v254, 9
	v_readlane_b32 s50, v254, 10
	v_readlane_b32 s51, v254, 11
	v_readlane_b32 s41, v255, 43
	s_waitcnt lgkmcnt(0)
	s_waitcnt vmcnt(13)
	v_pk_add_f32 v[18:19], v[24:25], 1.0 op_sel_hi:[1,0]
	v_pk_add_f32 v[22:23], v[22:23], 1.0 op_sel_hi:[1,0]
	s_waitcnt lgkmcnt(0)
	s_waitcnt vmcnt(11)
	v_pk_add_f32 v[24:25], v[26:27], v[94:95] op_sel_hi:[1,0] neg_lo:[0,1] neg_hi:[0,1]
	v_pk_add_f32 v[26:27], v[28:29], v[94:95] op_sel_hi:[1,0] neg_lo:[0,1] neg_hi:[0,1]
	s_waitcnt lgkmcnt(0)
	s_waitcnt vmcnt(10)
	v_pk_add_f32 v[28:29], v[30:31], v[94:95] op_sel_hi:[1,0] neg_lo:[0,1] neg_hi:[0,1]
	v_pk_add_f32 v[30:31], v[32:33], v[94:95] op_sel_hi:[1,0] neg_lo:[0,1] neg_hi:[0,1]
	s_waitcnt lgkmcnt(0)
	s_waitcnt vmcnt(9)
	v_pk_add_f32 v[32:33], v[34:35], v[94:95] op_sel_hi:[1,0] neg_lo:[0,1] neg_hi:[0,1]
	v_pk_add_f32 v[34:35], v[36:37], v[94:95] op_sel_hi:[1,0] neg_lo:[0,1] neg_hi:[0,1]
	s_waitcnt lgkmcnt(0)
	s_waitcnt vmcnt(8)
	v_pk_add_f32 v[36:37], v[38:39], v[94:95] op_sel_hi:[1,0] neg_lo:[0,1] neg_hi:[0,1]
	v_pk_add_f32 v[38:39], v[40:41], v[94:95] op_sel_hi:[1,0] neg_lo:[0,1] neg_hi:[0,1]
	v_pk_mul_f32 v[24:25], v[94:95], v[24:25] op_sel:[1,0]
	v_pk_mul_f32 v[38:39], v[94:95], v[38:39] op_sel:[1,0]
	s_waitcnt lgkmcnt(0)
	s_waitcnt vmcnt(0)
	v_pk_fma_f32 v[24:25], v[66:67], v[24:25], v[70:71]
	v_pk_mul_f32 v[32:33], v[94:95], v[32:33] op_sel:[1,0]
	v_pk_mul_f32 v[26:27], v[94:95], v[26:27] op_sel:[1,0]
	v_pk_fma_f32 v[38:39], v[38:39], v[48:49], v[44:45]
	v_pk_mul_f32 v[24:25], v[24:25], s[34:35] op_sel_hi:[1,0]
	v_pk_add_f32 v[8:9], v[8:9], 1.0 op_sel_hi:[1,0]
	v_pk_mul_f32 v[36:37], v[94:95], v[36:37] op_sel:[1,0]
	v_pk_fma_f32 v[32:33], v[32:33], v[50:51], v[54:55]
	v_pk_fma_f32 v[26:27], v[26:27], v[68:69], v[72:73]
	v_pk_mul_f32 v[38:39], v[38:39], s[34:35] op_sel_hi:[1,0]
	v_pk_fma_f32 v[54:55], v[78:79], v[22:23], v[24:25]
	v_pk_mul_f32 v[34:35], v[94:95], v[34:35] op_sel:[1,0]
	v_pk_mul_f32 v[28:29], v[94:95], v[28:29] op_sel:[1,0]
	v_pk_fma_f32 v[36:37], v[36:37], v[46:47], v[42:43]
	v_pk_mul_f32 v[26:27], v[26:27], s[34:35] op_sel_hi:[1,0]
	v_pk_fma_f32 v[42:43], v[84:85], v[8:9], v[38:39]
	v_add_f32_e32 v8, 0, v54
	v_pk_fma_f32 v[34:35], v[34:35], v[52:53], v[56:57]
	v_pk_fma_f32 v[28:29], v[28:29], v[62:63], v[58:59]
	v_pk_fma_f32 v[52:53], v[80:81], v[18:19], v[26:27]
	v_add_f32_e32 v8, v8, v55
	v_pk_add_f32 v[14:15], v[14:15], 1.0 op_sel_hi:[1,0]
	v_pk_mul_f32 v[30:31], v[94:95], v[30:31] op_sel:[1,0]
	v_pk_mul_f32 v[28:29], v[28:29], s[34:35] op_sel_hi:[1,0]
	v_add_f32_e32 v8, v8, v52
	v_pk_fma_f32 v[30:31], v[30:31], v[64:65], v[60:61]
	v_pk_fma_f32 v[50:51], v[82:83], v[14:15], v[28:29]
	v_add_f32_e32 v8, v8, v53
	v_pk_add_f32 v[16:17], v[16:17], 1.0 op_sel_hi:[1,0]
	v_pk_mul_f32 v[30:31], v[30:31], s[34:35] op_sel_hi:[1,0]
	v_add_f32_e32 v8, v8, v50
	v_pk_fma_f32 v[48:49], v[86:87], v[16:17], v[30:31]
	v_add_f32_e32 v8, v8, v51
	v_pk_add_f32 v[10:11], v[10:11], 1.0 op_sel_hi:[1,0]
	v_pk_mul_f32 v[32:33], v[32:33], s[34:35] op_sel_hi:[1,0]
	v_add_f32_e32 v8, v8, v48
	v_pk_fma_f32 v[46:47], v[88:89], v[10:11], v[32:33]
	v_add_f32_e32 v8, v8, v49
	v_pk_add_f32 v[12:13], v[12:13], 1.0 op_sel_hi:[1,0]
	v_pk_mul_f32 v[34:35], v[34:35], s[34:35] op_sel_hi:[1,0]
	v_add_f32_e32 v8, v8, v46
	v_pk_fma_f32 v[44:45], v[90:91], v[12:13], v[34:35]
	v_add_f32_e32 v8, v8, v47
	v_pk_add_f32 v[6:7], v[6:7], 1.0 op_sel_hi:[1,0]
	v_pk_mul_f32 v[36:37], v[36:37], s[34:35] op_sel_hi:[1,0]
	v_add_f32_e32 v8, v8, v44
	v_pk_fma_f32 v[6:7], v[92:93], v[6:7], v[36:37]
	v_add_f32_e32 v8, v8, v45
	v_add_f32_e32 v8, v8, v6
	v_add_f32_e32 v8, v8, v7
	v_add_f32_e32 v8, v8, v42
	v_add_f32_e32 v8, v8, v43
	ds_bpermute_b32 v9, v2, v8
	v_lshl_add_u64 v[22:23], s[12:13], 0, v[4:5]
	v_lshl_add_u64 v[38:39], s[90:91], 0, v[4:5]
	s_waitcnt lgkmcnt(0)
	v_add_f32_e32 v8, v8, v9
	ds_bpermute_b32 v9, v1, v8
	s_waitcnt lgkmcnt(0)
	v_add_f32_e32 v8, v8, v9
	ds_bpermute_b32 v9, v74, v8
	s_waitcnt lgkmcnt(0)
	v_add_f32_e32 v8, v8, v9
	ds_bpermute_b32 v9, v75, v8
	s_waitcnt lgkmcnt(0)
	v_add_f32_e32 v26, v8, v9
	ds_bpermute_b32 v27, v126, v26
	ds_read_b128 v[8:11], v185 offset:11264
	global_load_dword v184, v187, s[12:13]
	ds_read_b128 v[12:15], v185 offset:10240
	global_load_dword v184, v187, s[12:13]
	ds_read_b128 v[16:19], v185 offset:9216
	global_load_dword v184, v187, s[12:13]
	s_nop 0
	ds_read_b128 v[22:25], v185 offset:8192
	global_load_dword v184, v187, s[12:13]
	s_waitcnt lgkmcnt(0)
	v_add_f32_e32 v56, v26, v27
	ds_read_b128 v[26:29], v185 offset:15360
	global_load_dword v184, v187, s[90:91]
	ds_read_b128 v[30:33], v185 offset:14336
	global_load_dword v184, v187, s[90:91]
	ds_read_b128 v[34:37], v185 offset:13312
	global_load_dword v184, v187, s[90:91]
	s_nop 0
	ds_read_b128 v[38:41], v185 offset:12288
	global_load_dword v184, v187, s[90:91]
	ds_bpermute_b32 v57, v127, v56
	s_waitcnt lgkmcnt(0)
	v_add_f32_e32 v56, v56, v57
	v_mul_f32_e32 v56, 0x3a800000, v56
	v_pk_add_f32 v[54:55], v[54:55], v[56:57] op_sel_hi:[1,0] neg_lo:[0,1] neg_hi:[0,1]
	v_pk_add_f32 v[52:53], v[52:53], v[56:57] op_sel_hi:[1,0] neg_lo:[0,1] neg_hi:[0,1]
	v_pk_add_f32 v[50:51], v[50:51], v[56:57] op_sel_hi:[1,0] neg_lo:[0,1] neg_hi:[0,1]
	v_pk_add_f32 v[48:49], v[48:49], v[56:57] op_sel_hi:[1,0] neg_lo:[0,1] neg_hi:[0,1]
	v_pk_add_f32 v[46:47], v[46:47], v[56:57] op_sel_hi:[1,0] neg_lo:[0,1] neg_hi:[0,1]
	v_pk_add_f32 v[44:45], v[44:45], v[56:57] op_sel_hi:[1,0] neg_lo:[0,1] neg_hi:[0,1]
	v_pk_add_f32 v[6:7], v[6:7], v[56:57] op_sel_hi:[1,0] neg_lo:[0,1] neg_hi:[0,1]
	v_pk_add_f32 v[42:43], v[42:43], v[56:57] op_sel_hi:[1,0] neg_lo:[0,1] neg_hi:[0,1]
	v_pk_mul_f32 v[56:57], v[54:55], v[54:55]
	v_pk_mul_f32 v[58:59], v[52:53], v[52:53]
	v_add_f32_e32 v56, v56, v57
	v_add_f32_e32 v56, v58, v56
	v_pk_mul_f32 v[60:61], v[50:51], v[50:51]
	v_add_f32_e32 v56, v59, v56
	v_add_f32_e32 v56, v60, v56
	v_pk_mul_f32 v[62:63], v[48:49], v[48:49]
	v_add_f32_e32 v56, v61, v56
	v_add_f32_e32 v56, v62, v56
	v_pk_mul_f32 v[64:65], v[46:47], v[46:47]
	v_add_f32_e32 v56, v63, v56
	v_add_f32_e32 v56, v64, v56
	v_pk_mul_f32 v[66:67], v[44:45], v[44:45]
	v_add_f32_e32 v56, v65, v56
	v_add_f32_e32 v56, v66, v56
	v_pk_mul_f32 v[68:69], v[6:7], v[6:7]
	v_add_f32_e32 v56, v67, v56
	v_add_f32_e32 v56, v68, v56
	v_pk_mul_f32 v[70:71], v[42:43], v[42:43]
	v_add_f32_e32 v56, v69, v56
	v_add_f32_e32 v56, v70, v56
	v_add_f32_e32 v56, v71, v56
	ds_bpermute_b32 v2, v2, v56
	s_waitcnt lgkmcnt(0)
	v_add_f32_e32 v2, v56, v2
	ds_bpermute_b32 v1, v1, v2
	v_lshl_add_u64 v[56:57], s[20:21], 0, v[4:5]
	s_waitcnt lgkmcnt(0)
	v_add_f32_e32 v1, v2, v1
	ds_bpermute_b32 v2, v74, v1
	s_waitcnt lgkmcnt(0)
	v_add_f32_e32 v1, v1, v2
	ds_bpermute_b32 v2, v75, v1
	s_waitcnt lgkmcnt(0)
	v_add_f32_e32 v1, v1, v2
	ds_bpermute_b32 v2, v126, v1
	s_waitcnt lgkmcnt(0)
	v_add_f32_e32 v1, v1, v2
	ds_bpermute_b32 v2, v127, v1
	s_waitcnt lgkmcnt(0)
	v_add_f32_e32 v1, v1, v2
	v_fmamk_f32 v1, v1, 0x3a800000, v204
	v_mul_f32_e32 v2, 0x4b800000, v1
	v_cmp_gt_f32_e64 s[0:1], s42, v1
	s_nop 1
	v_cndmask_b32_e64 v1, v1, v2, s[0:1]
	v_rsq_f32_e32 v1, v1
	s_nop 0
	v_mul_f32_e32 v2, 0x45800000, v1
	v_cndmask_b32_e64 v2, v1, v2, s[0:1]
	v_pk_mul_f32 v[4:5], v[54:55], v[2:3] op_sel_hi:[1,0]
	v_pk_mul_f32 v[52:53], v[52:53], v[2:3] op_sel_hi:[1,0]
	v_pk_mul_f32 v[50:51], v[50:51], v[2:3] op_sel_hi:[1,0]
	v_pk_mul_f32 v[48:49], v[48:49], v[2:3] op_sel_hi:[1,0]
	v_pk_mul_f32 v[46:47], v[46:47], v[2:3] op_sel_hi:[1,0]
	v_pk_mul_f32 v[44:45], v[44:45], v[2:3] op_sel_hi:[1,0]
	v_pk_mul_f32 v[54:55], v[6:7], v[2:3] op_sel_hi:[1,0]
	v_pk_mul_f32 v[42:43], v[42:43], v[2:3] op_sel_hi:[1,0]
	s_waitcnt lgkmcnt(0)
	s_waitcnt vmcnt(0)
	v_pk_fma_f32 v[4:5], v[22:23], v[4:5], v[38:39]
	v_pk_fma_f32 v[6:7], v[24:25], v[52:53], v[40:41]
	v_pk_fma_f32 v[16:17], v[16:17], v[50:51], v[34:35]
	v_pk_fma_f32 v[18:19], v[18:19], v[48:49], v[36:37]
	v_pk_fma_f32 v[12:13], v[12:13], v[46:47], v[30:31]
	v_pk_fma_f32 v[14:15], v[14:15], v[44:45], v[32:33]
	v_pk_fma_f32 v[8:9], v[8:9], v[54:55], v[26:27]
	v_pk_fma_f32 v[10:11], v[10:11], v[42:43], v[28:29]
	global_store_dwordx4 v[56:57], v[4:7], off
	global_store_dwordx4 v[56:57], v[16:19], off offset:16
	global_store_dwordx4 v[56:57], v[12:15], off offset:32
	global_store_dwordx4 v[56:57], v[8:11], off offset:48
	s_cbranch_vccnz .LBB0_937
	s_lshl_b64 s[0:1], s[22:23], 10
	s_mul_hi_i32 s3, s2, 0x6000
	s_mulk_i32 s2, 0x6000
	s_add_u32 s2, s70, s2
	s_addc_u32 s3, s71, s3
	v_lshl_add_u64 v[50:51], v[20:21], 2, s[2:3]
	s_mov_b64 s[2:3], 0x19000
	v_add_co_u32_e32 v34, vcc, s86, v50
	v_lshl_add_u64 v[30:31], v[50:51], 0, s[2:3]
	s_mov_b64 s[2:3], 0x18000
	v_addc_co_u32_e32 v35, vcc, 0, v51, vcc
	v_lshl_add_u64 v[46:47], v[50:51], 0, s[2:3]
	v_add_co_u32_e32 v50, vcc, s67, v50
	global_load_dwordx4 v[22:25], v[30:31], off offset:32
	global_load_dwordx4 v[26:29], v[30:31], off offset:16
	v_addc_co_u32_e32 v51, vcc, 0, v51, vcc
	global_load_dwordx4 v[30:33], v[30:31], off offset:48
	s_nop 0
	global_load_dwordx4 v[34:37], v[34:35], off
	s_nop 0
	global_load_dwordx4 v[38:41], v[46:47], off offset:16
	global_load_dwordx4 v[42:45], v[46:47], off offset:48
	s_nop 0
	global_load_dwordx4 v[46:49], v[46:47], off offset:32
	s_lshl_b64 s[0:1], s[0:1], 1
	global_load_dwordx4 v[50:53], v[50:51], off
	s_add_u32 s0, s76, s0
	s_addc_u32 s1, s77, s1
	v_lshl_add_u64 v[20:21], v[20:21], 1, s[0:1]
	s_waitcnt lgkmcnt(0)
	s_waitcnt vmcnt(7)
	v_pk_add_f32 v[22:23], v[22:23], 1.0 op_sel_hi:[1,0]
	s_waitcnt lgkmcnt(0)
	s_waitcnt vmcnt(6)
	v_pk_add_f32 v[26:27], v[26:27], 1.0 op_sel_hi:[1,0]
	v_pk_add_f32 v[28:29], v[28:29], 1.0 op_sel_hi:[1,0]
	s_waitcnt lgkmcnt(0)
	s_waitcnt vmcnt(4)
	v_pk_add_f32 v[34:35], v[34:35], 1.0 op_sel_hi:[1,0]
	v_pk_add_f32 v[36:37], v[36:37], 1.0 op_sel_hi:[1,0]
	v_pk_add_f32 v[24:25], v[24:25], 1.0 op_sel_hi:[1,0]
	v_pk_add_f32 v[30:31], v[30:31], 1.0 op_sel_hi:[1,0]
	v_pk_add_f32 v[32:33], v[32:33], 1.0 op_sel_hi:[1,0]
	s_waitcnt lgkmcnt(0)
	s_waitcnt vmcnt(3)
	v_pk_fma_f32 v[16:17], v[16:17], v[26:27], v[38:39]
	v_pk_fma_f32 v[18:19], v[18:19], v[28:29], v[40:41]
	s_waitcnt lgkmcnt(0)
	s_waitcnt vmcnt(0)
	v_pk_fma_f32 v[4:5], v[4:5], v[34:35], v[50:51]
	v_pk_fma_f32 v[26:27], v[6:7], v[36:37], v[52:53]
	v_pk_fma_f32 v[12:13], v[12:13], v[22:23], v[46:47]
	v_pk_fma_f32 v[14:15], v[14:15], v[24:25], v[48:49]
	v_pk_fma_f32 v[22:23], v[8:9], v[30:31], v[42:43]
	v_pk_fma_f32 v[24:25], v[10:11], v[32:33], v[44:45]
	v_cvt_pk_bf16_f32 v6, v16, v17
	v_cvt_pk_bf16_f32 v7, v18, v19
	v_cvt_pk_bf16_f32 v4, v4, v5
	v_cvt_pk_bf16_f32 v5, v26, v27
	v_cvt_pk_bf16_f32 v8, v12, v13
	v_cvt_pk_bf16_f32 v9, v14, v15
	v_cvt_pk_bf16_f32 v10, v22, v23
	v_cvt_pk_bf16_f32 v11, v24, v25
	global_store_dwordx4 v[20:21], v[4:7], off
	global_store_dwordx4 v[20:21], v[8:11], off offset:16
	s_branch .LBB0_937
